# P4: each workgroup touches its 256x256 residual-input tile (one dword per 64 B, 8 loads per wave) during the out-projection K-loop so the epilogue reads it from cache
# baseline (speedup 1.0000x reference)
; #define PG8_BAR __builtin_amdgcn_s_barrier()
; template <class Epi, class Sched, bool ALIGN_EPI = false, bool SP2 = false, bool FP8 = false, bool PEEL = false>
; __device__ __forceinline__ void gemm_phase(PG8_LAS unsigned char* lds, const Gemm g, const Sched& S, const Epi& E, const int wid) {
;     const int lane = pg8_lane_id(), tid = wid * 64 + lane, wr = wid >> 2, wc = wid & 3, fr = lane & 15, fq = lane >> 4;
;     const int K = g.K, nt = g.nt ? g.nt : K / BK;
;     unsigned voffA[2], voffB[2];
; #pragma unroll
;     for (int i = 0; i < 2; ++i) { int R, C; stage_rc(tid * 16 + i * 8192, R, C); const int Rb = Epi::PERM ? ((R & ~31) + perm32(R & 31)) : R;
;         voffA[i] = (unsigned)(R * K + C) * 2u; voffB[i] = (unsigned)(Rb * K + C) * 2u; }
;     const size_t kstep = (size_t)(BK * 2);
;     const size_t hstep = (size_t)HALF * K * 2;
;     const size_t tstep = 2 * hstep;
;     const unsigned ldsw = (unsigned)wid * 1024u;
;     const int aoff = lds_byte(wr * 64 + fr, fq * 8), boff = lds_byte(wc * 32 + fr, fq * 8);
;     ...
;     Unit cur, nxt; int ui = 0;
;     if (!S.next(0, cur)) return;
;     f32x4 acc[2][2][4][2];
;     if constexpr (!PEEL) {
; #pragma unroll
;     for (int a = 0; a < 2; ++a)
; #pragma unroll
;         for (int b = 0; b < 2; ++b)
; #pragma unroll
;             for (int m = 0; m < 4; ++m)
; #pragma unroll
;                 for (int n = 0; n < 2; ++n) acc[a][b][m][n] = (f32x4){0.f, 0.f, 0.f, 0.f};
;     }
;     bf16x8 At[4][2], B0[2][2], B1[2][2]; i32x8 At8[4], B08[2], B18[2];
;     const char* cA = (const char*)g.A + (size_t)cur.pm * tstep + cur.koff; const char* cB = (const char*)g.Bt + (size_t)cur.pn * tstep + cur.koff;
;     S.a_ready(cur);
;     if constexpr (SP2) {
;         PG8_STAGE(PG8_SB(0, 0), cB, voffB); PG8_STAGE(PG8_SB(0, 1), cB + hstep, voffB); PG8_STAGE(PG8_SA(0, 0), cA, voffA); PG8_STAGE(PG8_SA(0, 1), cA + hstep, voffA);
;         if (wr == 1) PG8_BAR;
;         PG8_WAIT_V(2); PG8_BAR;
;         PG8_STAGE(PG8_SB(1, 0), cB + kstep, voffB); PG8_STAGE(PG8_SA(1, 0), cA + kstep, voffA); PG8_STAGE(PG8_SB(1, 1), cB + hstep + kstep, voffB);
;         PG8_WAIT_V(6); PG8_BAR;
;     } else {
;         PG8_STAGE(PG8_SB(0, 0), cB, voffB); PG8_STAGE(PG8_SA(0, 0), cA, voffA); PG8_STAGE(PG8_SB(0, 1), cB + hstep, voffB); PG8_STAGE(PG8_SA(0, 1), cA + hstep, voffA);
;         if (wr == 1) PG8_BAR;
;         PG8_WAIT_V(4); PG8_BAR;
.LBB0_647:
	s_cmp_lt_i32 s80, 5
	s_cselect_b64 s[4:5], -1, 0
	s_add_u32 s18, s78, 0x7a00000
	s_addc_u32 s19, s79, 0
	s_and_b64 s[0:1], s[4:5], s[0:1]
	s_andn2_b64 vcc, exec, s[0:1]
	s_cbranch_vccnz .LBB0_741
	s_cmpk_gt_i32 s2, 0xff
	v_mbcnt_lo_u32_b32 v187, -1, 0
	v_mbcnt_hi_u32_b32 v187, -1, v187
	s_cbranch_scc1 .LBB0_741
	s_add_u32 s37, s78, 0xa00000
	s_addc_u32 s40, s79, 0
	s_lshl_b32 s41, s96, 10
	v_lshlrev_b32_e32 v188, 4, v187
	v_add_u32_e32 v0, s41, v188
	s_waitcnt lgkmcnt(0)
	v_add_u32_e32 v1, 0x2000, v0
	v_ashrrev_i32_e32 v2, 31, v1
	v_lshrrev_b32_e32 v2, 22, v2
	v_add_u32_e32 v2, v1, v2
	v_ashrrev_i32_e32 v8, 10, v2
	v_mul_i32_i24_e32 v2, 0x400, v8
	v_sub_u32_e32 v1, v1, v2
	v_lshrrev_b32_e32 v2, 4, v1
	v_bitop3_b32 v1, v2, v1, 32 bitop3:0x6c
	v_ashrrev_i32_e32 v2, 31, v1
	v_lshrrev_b32_e32 v2, 26, v2
	v_add_u32_e32 v2, v1, v2
	v_ashrrev_i32_e32 v9, 6, v2
	v_lshlrev_b32_e32 v3, 3, v8
	v_and_b32_e32 v2, 0xffc0, v2
	v_and_b32_e32 v3, -16, v3
	v_sub_u32_e32 v1, v1, v2
	v_add_u32_e32 v3, v9, v3
	v_lshrrev_b16_e32 v2, 7, v1
	v_and_b32_e32 v4, 3, v9
	s_mov_b32 s3, 0x1fffe0
	v_lshrrev_b32_e32 v5, 2, v3
	v_lshlrev_b32_e32 v6, 1, v3
	v_and_b32_e32 v2, 1, v2
	v_and_or_b32 v4, v3, s3, v4
	v_and_b32_e32 v5, 4, v5
	v_and_b32_e32 v6, 24, v6
	v_add_u16_e32 v1, v1, v2
	v_mov_b32_e32 v2, 1
	v_or3_b32 v4, v4, v5, v6
	v_lshlrev_b32_e32 v5, 5, v8
	v_ashrrev_i16_sdwa v1, v2, sext(v1) dst_sel:DWORD dst_unused:UNUSED_PAD src0_sel:DWORD src1_sel:BYTE_0
	v_and_b32_e32 v5, 32, v5
	v_bfe_i32 v10, v1, 0, 16
	v_add_lshl_u32 v1, v5, v10, 1
	v_lshl_add_u32 v128, v4, 11, v1
	v_lshl_add_u32 v130, v3, 11, v1
	v_ashrrev_i32_e32 v1, 31, v0
	v_lshrrev_b32_e32 v1, 22, v1
	v_add_u32_e32 v1, v0, v1
	v_ashrrev_i32_e32 v11, 10, v1
	v_mul_i32_i24_e32 v1, 0x400, v11
	v_sub_u32_e32 v0, v0, v1
	v_lshrrev_b32_e32 v1, 4, v0
	v_bitop3_b32 v0, v1, v0, 32 bitop3:0x6c
	v_ashrrev_i32_e32 v1, 31, v0
	v_lshrrev_b32_e32 v1, 26, v1
	v_add_u32_e32 v1, v0, v1
	v_lshlrev_b32_e32 v3, 3, v11
	v_ashrrev_i32_e32 v12, 6, v1
	v_and_b32_e32 v3, -16, v3
	v_add_u32_e32 v3, v12, v3
	v_and_b32_e32 v4, 3, v12
	s_ashr_i32 s42, s2, 31
	v_and_or_b32 v4, v3, s3, v4
	s_lshr_b32 s3, s42, 29
	s_add_i32 s3, s2, s3
	s_and_b32 s4, s3, -8
	s_sub_i32 s4, s2, s4
	s_lshr_b32 s5, s94, 8
	s_lshl_b32 s7, s4, 5
	s_ashr_i32 s3, s3, 3
	s_mul_i32 s6, s4, 33
	s_cmp_lt_i32 s4, 0
	s_cselect_b32 s4, s6, s7
	s_add_i32 s3, s4, s3
	s_ashr_i32 s4, s3, 31
	s_lshr_b32 s4, s4, 27
	s_add_i32 s4, s3, s4
	s_ashr_i32 s6, s4, 5
	s_and_b32 s4, s4, 0xffe0
	s_sub_i32 s3, s3, s4
	s_bfe_i32 s4, s3, 0x80000
	s_bfe_u32 s4, s4, 0x3000c
	s_add_i32 s7, s3, s4
	s_bfe_i32 s4, s7, 0x80000
	s_and_b32 s7, s7, 0xf8
	s_sub_i32 s3, s3, s7
	s_lshl_b32 s6, s6, 3
	s_sext_i32_i16 s4, s4
	s_sext_i32_i8 s3, s3
	s_lshr_b32 s4, s4, 3
	s_add_i32 s8, s6, s3
	v_lshrrev_b32_e32 v5, 2, v3
	v_lshlrev_b32_e32 v6, 1, v3
	v_and_b32_e32 v1, 0xc0, v1
	s_ashr_i32 s9, s8, 31
	s_bfe_i64 s[10:11], s[4:5], 0x100000
	v_and_b32_e32 v5, 4, v5
	v_and_b32_e32 v6, 24, v6
	v_sub_u32_e32 v0, v0, v1
	s_lshl_b64 s[6:7], s[8:9], 19
	s_lshl_b64 s[10:11], s[10:11], 19
	v_or3_b32 v4, v4, v5, v6
	v_lshlrev_b32_e32 v5, 5, v11
	v_ashrrev_i16_sdwa v0, v2, sext(v0) dst_sel:DWORD dst_unused:UNUSED_PAD src0_sel:DWORD src1_sel:BYTE_0
	s_add_u32 s24, s37, s10
	v_and_b32_e32 v5, 32, v5
	v_bfe_i32 v13, v0, 0, 16
	s_addc_u32 s25, s40, s11
	s_add_i32 s43, s41, 0
	v_add_lshl_u32 v0, v5, v13, 1
	s_add_i32 m0, s43, 0x10000
	s_add_i32 s3, s43, 0x12000
	v_lshl_add_u32 v132, v4, 11, v0
	s_add_u32 s10, s24, 0x40000
	s_addc_u32 s11, s25, 0
	s_add_i32 s9, s43, 0x14000
	s_add_i32 s14, s43, 0x16000
	v_readlane_b32 s98, v254, 36
	v_readlane_b32 s99, v254, 37
	s_lshl_b32 s100, s8, 20
	s_add_u32 s98, s98, s100
	s_addc_u32 s99, s99, 0
	s_sext_i32_i16 s100, s4
	s_lshl_b32 s100, s100, 10
	s_add_u32 s98, s98, s100
	s_addc_u32 s99, s99, 0
	v_lshrrev_b32_e32 v250, 4, v187
	s_lshl_b32 s100, s96, 5
	v_add_u32_e32 v250, s100, v250
	v_lshlrev_b32_e32 v250, 12, v250
	v_and_b32_e32 v251, 15, v187
	v_lshl_add_u32 v250, v251, 6, v250
	global_load_lds_dwordx4 v132, s[24:25]
	s_mov_b32 m0, s3
	s_add_u32 s6, s34, s6
	global_load_lds_dwordx4 v128, s[24:25]
	s_mov_b32 m0, s9
	s_addc_u32 s7, s35, s7
	s_add_i32 s44, s43, 0x2000
	global_load_lds_dwordx4 v132, s[10:11]
	s_mov_b32 m0, s14
	v_lshl_add_u32 v134, v3, 11, v0
	s_add_u32 s12, s6, 0x40000
	global_load_lds_dwordx4 v128, s[10:11]
	s_mov_b32 m0, s43
	s_addc_u32 s13, s7, 0
	s_add_i32 s45, s43, 0x4000
	global_load_lds_dwordx4 v134, s[6:7]
	s_mov_b32 m0, s44
	s_add_i32 s46, s43, 0x6000
	global_load_lds_dwordx4 v130, s[6:7]
	s_mov_b32 m0, s45
	v_mov_b32_e32 v133, 0
	global_load_lds_dwordx4 v134, s[12:13]
	s_mov_b32 m0, s46
	v_mov_b32_e32 v129, v133
	global_load_lds_dwordx4 v130, s[12:13]
	v_mov_b32_e32 v135, v133
	v_mov_b32_e32 v131, v133
	s_cmp_lg_u32 s5, 1
	v_lshl_add_u64 v[6:7], s[24:25], 0, v[132:133]
	v_lshl_add_u64 v[4:5], s[24:25], 0, v[128:129]
	v_lshl_add_u64 v[2:3], s[6:7], 0, v[134:135]
	v_lshl_add_u64 v[0:1], s[6:7], 0, v[130:131]
	s_cbranch_scc1 .LBB0_651
	s_barrier

; #define PG8_STAGE(bufoff, gbase, voff) do { _Pragma("unroll") for (int _i = 0; _i < 2; ++_i) \
;         __builtin_amdgcn_global_load_lds((const unsigned*)((const char*)(gbase) + (voff)[_i]), (PG8_LAS unsigned*)(lds + (bufoff) + ldsw + _i * 8192), 16, 0, 0); } while (0)
; #define PG8_WAIT_V(n) asm volatile("s_waitcnt vmcnt(" #n ")" ::: "memory")
; #define PG8_WAIT_L(n) asm volatile("s_waitcnt lgkmcnt(" #n ")" ::: "memory")
; #define PG8_BAR __builtin_amdgcn_s_barrier()
; #define PG8_SCHED __builtin_amdgcn_sched_barrier(0)
; template <class Epi, class Sched, bool ALIGN_EPI = false, bool SP2 = false, bool FP8 = false, bool PEEL = false>
; __device__ __forceinline__ void gemm_phase(PG8_LAS unsigned char* lds, const Gemm g, const Sched& S, const Epi& E, const int wid) {
;     ...
;         for (int t = 0; t < nt; t += 2) {
;             const bool last = (t == nt - 2);
;             const char* a1 = cA + (size_t)(t + 1) * kstep;
;             const char* a2 = last ? nA : cA + (size_t)(t + 2) * kstep; const char* b2 = last ? nB : cB + (size_t)(t + 2) * kstep;
;             const char* a3 = a2 + kstep; const char* b3 = b2 + kstep;
;             if (last && has_next) S.a_ready(nxt);
;             PG8_LDB(B0, 0, 0); PG8_LDB(B1, 0, 1); PG8_SCHED; PG8_LDA(At, 0, 0); PG8_STAGE(PG8_SA(1, 1), a1 + hstep, voffA);
;             PG8_WAIT_V(8); PG8_WAIT_L(0); PG8_BAR; PG8_MMA(0, 0, At, B0); PG8_MMA(0, 1, At, B1); PG8_BAR; PG8_SCHED;
;             PG8_LDA(At, 0, 1); PG8_STAGE(PG8_SB(0, 0), b2, voffB); PG8_STAGE(PG8_SB(0, 1), b2 + hstep, voffB); PG8_STAGE(PG8_SA(0, 0), a2, voffA);
;             PG8_WAIT_V(8); PG8_WAIT_L(0); PG8_BAR; PG8_MMA(1, 0, At, B0); PG8_MMA(1, 1, At, B1); PG8_BAR; PG8_SCHED;
.LBB0_659:
	global_load_dword v251, v250, s[98:99]
	s_add_u32 s98, s98, 0x4000
	s_addc_u32 s99, s99, 0
	v_add_u32_e32 v162, s50, v148
	v_add_u32_e32 v178, s51, v148
	s_add_u32 s26, s6, s24
	ds_read_b128 v[150:153], v162
	ds_read_b128 v[154:157], v162 offset:1024
	ds_read_b128 v[158:161], v162 offset:2048
	ds_read_b128 v[162:165], v162 offset:3072
	ds_read_b128 v[166:169], v178
	ds_read_b128 v[170:173], v178 offset:1024
	ds_read_b128 v[174:177], v178 offset:2048
	ds_read_b128 v[178:181], v178 offset:3072
	s_addc_u32 s27, s7, s25
	s_add_u32 s26, s26, 0x100
	s_addc_u32 s27, s27, 0
	s_add_u32 s59, s54, s24
	s_addc_u32 s60, s55, s25
	s_cmpk_eq_i32 s24, 0x700
	s_cselect_b32 s31, s17, s27
	s_cselect_b32 s30, s56, s26
	s_cselect_b32 s27, s15, s60
	s_cselect_b32 s26, s57, s59
	v_lshl_add_u64 v[218:219], v[144:145], 0, s[24:25]
	s_add_i32 m0, s43, 0xc000
	ds_read_b128 v[182:185], v149
	ds_read_b128 v[190:193], v149 offset:1024
	ds_read_b128 v[194:197], v149 offset:2048
	ds_read_b128 v[198:201], v149 offset:3072
	ds_read_b128 v[202:205], v149 offset:4096
	ds_read_b128 v[206:209], v149 offset:5120
	ds_read_b128 v[210:213], v149 offset:6144
	ds_read_b128 v[214:217], v149 offset:7168
	global_load_lds_dwordx4 v[218:219], off
	v_lshl_add_u64 v[218:219], v[146:147], 0, s[24:25]
	s_add_i32 m0, s43, 0xe000
	s_nop 0
	global_load_lds_dwordx4 v[218:219], off
	s_waitcnt vmcnt(9)
	s_waitcnt lgkmcnt(0)
	s_barrier
	s_setprio 1
	s_waitcnt lgkmcnt(0)
	v_mfma_f32_16x16x32_bf16 v[124:127], v[150:153], v[182:185], v[124:127]
	v_mfma_f32_16x16x32_bf16 v[120:123], v[158:161], v[182:185], v[120:123]
	v_mfma_f32_16x16x32_bf16 v[112:115], v[150:153], v[194:197], v[112:115]
	v_mfma_f32_16x16x32_bf16 v[108:111], v[158:161], v[194:197], v[108:111]
	v_mfma_f32_16x16x32_bf16 v[100:103], v[150:153], v[202:205], v[100:103]
	v_mfma_f32_16x16x32_bf16 v[92:95], v[158:161], v[202:205], v[92:95]
	v_mfma_f32_16x16x32_bf16 v[84:87], v[150:153], v[210:213], v[84:87]
	v_mfma_f32_16x16x32_bf16 v[76:79], v[158:161], v[210:213], v[76:79]
	v_mfma_f32_16x16x32_bf16 v[124:127], v[154:157], v[190:193], v[124:127]
	v_mfma_f32_16x16x32_bf16 v[120:123], v[162:165], v[190:193], v[120:123]
	v_mfma_f32_16x16x32_bf16 v[112:115], v[154:157], v[198:201], v[112:115]
	v_mfma_f32_16x16x32_bf16 v[108:111], v[162:165], v[198:201], v[108:111]
	v_mfma_f32_16x16x32_bf16 v[100:103], v[154:157], v[206:209], v[100:103]
	v_mfma_f32_16x16x32_bf16 v[92:95], v[162:165], v[206:209], v[92:95]
	v_mfma_f32_16x16x32_bf16 v[84:87], v[154:157], v[214:217], v[84:87]
	v_mfma_f32_16x16x32_bf16 v[76:79], v[162:165], v[214:217], v[76:79]
	s_setprio 0
	s_setprio 1
	v_mfma_f32_16x16x32_bf16 v[116:119], v[166:169], v[182:185], v[116:119]
	v_mfma_f32_16x16x32_bf16 v[104:107], v[174:177], v[182:185], v[104:107]
	v_mfma_f32_16x16x32_bf16 v[96:99], v[166:169], v[194:197], v[96:99]
	v_mfma_f32_16x16x32_bf16 v[88:91], v[174:177], v[194:197], v[88:91]
	v_mfma_f32_16x16x32_bf16 v[80:83], v[166:169], v[202:205], v[80:83]
	v_mfma_f32_16x16x32_bf16 v[72:75], v[174:177], v[202:205], v[72:75]
	v_mfma_f32_16x16x32_bf16 v[68:71], v[166:169], v[210:213], v[68:71]
	v_mfma_f32_16x16x32_bf16 v[64:67], v[174:177], v[210:213], v[64:67]
	v_mfma_f32_16x16x32_bf16 v[116:119], v[170:173], v[190:193], v[116:119]
	v_mfma_f32_16x16x32_bf16 v[104:107], v[178:181], v[190:193], v[104:107]
	v_mfma_f32_16x16x32_bf16 v[96:99], v[170:173], v[198:201], v[96:99]
	v_mfma_f32_16x16x32_bf16 v[88:91], v[178:181], v[198:201], v[88:91]
	v_mfma_f32_16x16x32_bf16 v[80:83], v[170:173], v[206:209], v[80:83]
	v_mfma_f32_16x16x32_bf16 v[72:75], v[178:181], v[206:209], v[72:75]
	v_mfma_f32_16x16x32_bf16 v[68:71], v[170:173], v[214:217], v[68:71]
	v_mfma_f32_16x16x32_bf16 v[64:67], v[178:181], v[214:217], v[64:67]
	s_setprio 0
	s_barrier
	s_add_i32 s59, s50, s41
	v_lshl_add_u64 v[218:219], s[26:27], 0, v[132:133]
	s_mov_b32 m0, s59
	ds_read_b128 v[182:185], v149 offset:16384
	ds_read_b128 v[190:193], v149 offset:17408
	ds_read_b128 v[194:197], v149 offset:18432
	ds_read_b128 v[198:201], v149 offset:19456
	ds_read_b128 v[202:205], v149 offset:20480
	ds_read_b128 v[206:209], v149 offset:21504
	ds_read_b128 v[210:213], v149 offset:22528
	ds_read_b128 v[214:217], v149 offset:23552
	global_load_lds_dwordx4 v[218:219], off
	s_add_i32 m0, s59, 0x2000
	s_add_u32 s60, s26, 0x40000
	v_lshl_add_u64 v[220:221], s[26:27], 0, v[128:129]
	s_addc_u32 s61, s27, 0
	s_add_i32 s59, s51, s41
	global_load_lds_dwordx4 v[220:221], off
	v_lshl_add_u64 v[222:223], s[60:61], 0, v[132:133]
	s_mov_b32 m0, s59
	v_lshl_add_u64 v[224:225], s[30:31], 0, v[130:131]
	global_load_lds_dwordx4 v[222:223], off
	v_lshl_add_u64 v[222:223], s[60:61], 0, v[128:129]
	s_add_i32 m0, s59, 0x2000
	s_nop 0
	global_load_lds_dwordx4 v[222:223], off
	v_lshl_add_u64 v[222:223], s[30:31], 0, v[134:135]
	s_mov_b32 m0, s43
	s_nop 0
	global_load_lds_dwordx4 v[222:223], off
	s_mov_b32 m0, s44
	s_nop 0
	global_load_lds_dwordx4 v[224:225], off
	s_waitcnt vmcnt(9)
	s_waitcnt lgkmcnt(0)
	s_barrier
; #define PG8_STAGE(bufoff, gbase, voff) do { _Pragma("unroll") for (int _i = 0; _i < 2; ++_i) \
;         __builtin_amdgcn_global_load_lds((const unsigned*)((const char*)(gbase) + (voff)[_i]), (PG8_LAS unsigned*)(lds + (bufoff) + ldsw + _i * 8192), 16, 0, 0); } while (0)
; #define PG8_WAIT_V(n) asm volatile("s_waitcnt vmcnt(" #n ")" ::: "memory")
; #define PG8_WAIT_L(n) asm volatile("s_waitcnt lgkmcnt(" #n ")" ::: "memory")
; #define PG8_BAR __builtin_amdgcn_s_barrier()
; #define PG8_SCHED __builtin_amdgcn_sched_barrier(0)
; template <class Epi, class Sched, bool ALIGN_EPI = false, bool SP2 = false, bool FP8 = false, bool PEEL = false>
; __device__ __forceinline__ void gemm_phase(PG8_LAS unsigned char* lds, const Gemm g, const Sched& S, const Epi& E, const int wid) {
;     ...
;             PG8_WAIT_V(8); PG8_WAIT_L(0); PG8_BAR; PG8_MMA(1, 0, At, B0); PG8_MMA(1, 1, At, B1); PG8_BAR; PG8_SCHED;
;             PG8_LDB(B0, 1, 0); PG8_LDB(B1, 1, 1); PG8_SCHED; PG8_LDA(At, 1, 0); PG8_STAGE(PG8_SA(0, 1), a2 + hstep, voffA);
;             PG8_WAIT_V(8); PG8_WAIT_L(0); PG8_BAR; PG8_MMA(0, 0, At, B0); PG8_MMA(0, 1, At, B1); PG8_BAR; PG8_SCHED;
;             PG8_LDA(At, 1, 1); PG8_STAGE(PG8_SB(1, 0), b3, voffB); PG8_STAGE(PG8_SB(1, 1), b3 + hstep, voffB); PG8_STAGE(PG8_SA(1, 0), a3, voffA);
;             PG8_WAIT_V(8); PG8_WAIT_L(0); PG8_BAR; PG8_MMA(1, 0, At, B0); PG8_MMA(1, 1, At, B1); PG8_BAR; PG8_SCHED;
	s_setprio 1
	s_waitcnt lgkmcnt(0)
	v_mfma_f32_16x16x32_bf16 v[60:63], v[150:153], v[182:185], v[60:63]
	v_mfma_f32_16x16x32_bf16 v[56:59], v[158:161], v[182:185], v[56:59]
	v_mfma_f32_16x16x32_bf16 v[52:55], v[150:153], v[194:197], v[52:55]
	v_mfma_f32_16x16x32_bf16 v[44:47], v[158:161], v[194:197], v[44:47]
	v_mfma_f32_16x16x32_bf16 v[36:39], v[150:153], v[202:205], v[36:39]
	v_mfma_f32_16x16x32_bf16 v[28:31], v[158:161], v[202:205], v[28:31]
	v_mfma_f32_16x16x32_bf16 v[20:23], v[150:153], v[210:213], v[20:23]
	v_mfma_f32_16x16x32_bf16 v[12:15], v[158:161], v[210:213], v[12:15]
	v_mfma_f32_16x16x32_bf16 v[60:63], v[154:157], v[190:193], v[60:63]
	v_mfma_f32_16x16x32_bf16 v[56:59], v[162:165], v[190:193], v[56:59]
	v_mfma_f32_16x16x32_bf16 v[52:55], v[154:157], v[198:201], v[52:55]
	v_mfma_f32_16x16x32_bf16 v[44:47], v[162:165], v[198:201], v[44:47]
	v_mfma_f32_16x16x32_bf16 v[36:39], v[154:157], v[206:209], v[36:39]
	v_mfma_f32_16x16x32_bf16 v[28:31], v[162:165], v[206:209], v[28:31]
	v_mfma_f32_16x16x32_bf16 v[20:23], v[154:157], v[214:217], v[20:23]
	v_mfma_f32_16x16x32_bf16 v[12:15], v[162:165], v[214:217], v[12:15]
	s_setprio 0
	s_setprio 1
	v_mfma_f32_16x16x32_bf16 v[48:51], v[166:169], v[182:185], v[48:51]
	v_mfma_f32_16x16x32_bf16 v[40:43], v[174:177], v[182:185], v[40:43]
	v_mfma_f32_16x16x32_bf16 v[32:35], v[166:169], v[194:197], v[32:35]
	v_mfma_f32_16x16x32_bf16 v[24:27], v[174:177], v[194:197], v[24:27]
	v_mfma_f32_16x16x32_bf16 v[16:19], v[166:169], v[202:205], v[16:19]
	v_mfma_f32_16x16x32_bf16 v[8:11], v[174:177], v[202:205], v[8:11]
	v_mfma_f32_16x16x32_bf16 v[4:7], v[166:169], v[210:213], v[4:7]
	v_mfma_f32_16x16x32_bf16 v[0:3], v[174:177], v[210:213], v[0:3]
	v_mfma_f32_16x16x32_bf16 v[48:51], v[170:173], v[190:193], v[48:51]
	v_mfma_f32_16x16x32_bf16 v[40:43], v[178:181], v[190:193], v[40:43]
	v_mfma_f32_16x16x32_bf16 v[32:35], v[170:173], v[198:201], v[32:35]
	v_mfma_f32_16x16x32_bf16 v[24:27], v[178:181], v[198:201], v[24:27]
	v_mfma_f32_16x16x32_bf16 v[16:19], v[170:173], v[206:209], v[16:19]
	v_mfma_f32_16x16x32_bf16 v[8:11], v[178:181], v[206:209], v[8:11]
	v_mfma_f32_16x16x32_bf16 v[4:7], v[170:173], v[214:217], v[4:7]
	v_mfma_f32_16x16x32_bf16 v[0:3], v[178:181], v[214:217], v[0:3]
	s_setprio 0
	s_barrier
	s_add_i32 s59, 0, 0x18000
	s_add_i32 s60, 0, 0x1c000
	v_add_u32_e32 v162, s59, v148
	v_add_u32_e32 v178, s60, v148
	ds_read_b128 v[150:153], v162
	ds_read_b128 v[154:157], v162 offset:1024
	ds_read_b128 v[158:161], v162 offset:2048
	ds_read_b128 v[162:165], v162 offset:3072
	ds_read_b128 v[166:169], v178
	ds_read_b128 v[170:173], v178 offset:1024
	ds_read_b128 v[174:177], v178 offset:2048
	ds_read_b128 v[178:181], v178 offset:3072
	s_add_u32 s30, s30, 0x40000
	s_addc_u32 s31, s31, 0
	s_mov_b32 m0, s45
	v_lshl_add_u64 v[226:227], s[30:31], 0, v[134:135]
	ds_read_b128 v[182:185], v149 offset:32768
	ds_read_b128 v[190:193], v149 offset:33792
	ds_read_b128 v[194:197], v149 offset:34816
	ds_read_b128 v[198:201], v149 offset:35840
	ds_read_b128 v[202:205], v149 offset:36864
	ds_read_b128 v[206:209], v149 offset:37888
	ds_read_b128 v[210:213], v149 offset:38912
	ds_read_b128 v[214:217], v149 offset:39936
	global_load_lds_dwordx4 v[226:227], off
	v_lshl_add_u64 v[226:227], s[30:31], 0, v[130:131]
	s_mov_b32 m0, s46
	s_nop 0
	global_load_lds_dwordx4 v[226:227], off
	s_waitcnt vmcnt(8)
	s_waitcnt lgkmcnt(0)
	s_barrier
	s_setprio 1
	s_waitcnt lgkmcnt(0)
	v_mfma_f32_16x16x32_bf16 v[124:127], v[150:153], v[182:185], v[124:127]
	v_mfma_f32_16x16x32_bf16 v[120:123], v[158:161], v[182:185], v[120:123]
	v_mfma_f32_16x16x32_bf16 v[112:115], v[150:153], v[194:197], v[112:115]
	v_mfma_f32_16x16x32_bf16 v[108:111], v[158:161], v[194:197], v[108:111]
	v_mfma_f32_16x16x32_bf16 v[100:103], v[150:153], v[202:205], v[100:103]
	v_mfma_f32_16x16x32_bf16 v[92:95], v[158:161], v[202:205], v[92:95]
	v_mfma_f32_16x16x32_bf16 v[84:87], v[150:153], v[210:213], v[84:87]
	v_mfma_f32_16x16x32_bf16 v[76:79], v[158:161], v[210:213], v[76:79]
	v_mfma_f32_16x16x32_bf16 v[124:127], v[154:157], v[190:193], v[124:127]
	v_mfma_f32_16x16x32_bf16 v[120:123], v[162:165], v[190:193], v[120:123]
	v_mfma_f32_16x16x32_bf16 v[112:115], v[154:157], v[198:201], v[112:115]
	v_mfma_f32_16x16x32_bf16 v[108:111], v[162:165], v[198:201], v[108:111]
	v_mfma_f32_16x16x32_bf16 v[100:103], v[154:157], v[206:209], v[100:103]
	v_mfma_f32_16x16x32_bf16 v[92:95], v[162:165], v[206:209], v[92:95]
	v_mfma_f32_16x16x32_bf16 v[84:87], v[154:157], v[214:217], v[84:87]
	v_mfma_f32_16x16x32_bf16 v[76:79], v[162:165], v[214:217], v[76:79]
	s_setprio 0
	s_setprio 1
	v_mfma_f32_16x16x32_bf16 v[116:119], v[166:169], v[182:185], v[116:119]
	v_mfma_f32_16x16x32_bf16 v[104:107], v[174:177], v[182:185], v[104:107]
	v_mfma_f32_16x16x32_bf16 v[96:99], v[166:169], v[194:197], v[96:99]
	v_mfma_f32_16x16x32_bf16 v[88:91], v[174:177], v[194:197], v[88:91]
	v_mfma_f32_16x16x32_bf16 v[80:83], v[166:169], v[202:205], v[80:83]
	v_mfma_f32_16x16x32_bf16 v[72:75], v[174:177], v[202:205], v[72:75]
	v_mfma_f32_16x16x32_bf16 v[68:71], v[166:169], v[210:213], v[68:71]
	v_mfma_f32_16x16x32_bf16 v[64:67], v[174:177], v[210:213], v[64:67]
	v_mfma_f32_16x16x32_bf16 v[116:119], v[170:173], v[190:193], v[116:119]
	v_mfma_f32_16x16x32_bf16 v[104:107], v[178:181], v[190:193], v[104:107]
	v_mfma_f32_16x16x32_bf16 v[96:99], v[170:173], v[198:201], v[96:99]
	v_mfma_f32_16x16x32_bf16 v[88:91], v[178:181], v[198:201], v[88:91]
	v_mfma_f32_16x16x32_bf16 v[80:83], v[170:173], v[206:209], v[80:83]
	v_mfma_f32_16x16x32_bf16 v[72:75], v[178:181], v[206:209], v[72:75]
	v_mfma_f32_16x16x32_bf16 v[68:71], v[170:173], v[214:217], v[68:71]
	v_mfma_f32_16x16x32_bf16 v[64:67], v[178:181], v[214:217], v[64:67]
	s_setprio 0
	s_barrier
; #define PG8_STAGE(bufoff, gbase, voff) do { _Pragma("unroll") for (int _i = 0; _i < 2; ++_i) \
;         __builtin_amdgcn_global_load_lds((const unsigned*)((const char*)(gbase) + (voff)[_i]), (PG8_LAS unsigned*)(lds + (bufoff) + ldsw + _i * 8192), 16, 0, 0); } while (0)
; #define PG8_WAIT_V(n) asm volatile("s_waitcnt vmcnt(" #n ")" ::: "memory")
; #define PG8_WAIT_L(n) asm volatile("s_waitcnt lgkmcnt(" #n ")" ::: "memory")
; #define PG8_BAR __builtin_amdgcn_s_barrier()
; #define PG8_SCHED __builtin_amdgcn_sched_barrier(0)
; template <class Epi, class Sched, bool ALIGN_EPI = false, bool SP2 = false, bool FP8 = false, bool PEEL = false>
; __device__ __forceinline__ void gemm_phase(PG8_LAS unsigned char* lds, const Gemm g, const Sched& S, const Epi& E, const int wid) {
;     ...
;             PG8_LDA(At, 1, 1); PG8_STAGE(PG8_SB(1, 0), b3, voffB); PG8_STAGE(PG8_SB(1, 1), b3 + hstep, voffB); PG8_STAGE(PG8_SA(1, 0), a3, voffA);
;             PG8_WAIT_V(8); PG8_WAIT_L(0); PG8_BAR; PG8_MMA(1, 0, At, B0); PG8_MMA(1, 1, At, B1); PG8_BAR; PG8_SCHED;
;         }
;     ...
;         if constexpr (!PEEL) {
; #pragma unroll
;         for (int a = 0; a < 2; ++a)
; #pragma unroll
;             for (int b = 0; b < 2; ++b)
; #pragma unroll
;                 for (int m = 0; m < 4; ++m)
; #pragma unroll
;                     for (int n = 0; n < 2; ++n) acc[a][b][m][n] = (f32x4){0.f, 0.f, 0.f, 0.f};
;         }
;         cur = nxt; cA = nA; cB = nB; ++ui;
	s_add_i32 s30, s59, s41
	v_lshl_add_u64 v[218:219], v[218:219], 0, s[12:13]
	s_mov_b32 m0, s30
	ds_read_b128 v[182:185], v149 offset:49152
	ds_read_b128 v[190:193], v149 offset:50176
	ds_read_b128 v[194:197], v149 offset:51200
	ds_read_b128 v[198:201], v149 offset:52224
	ds_read_b128 v[202:205], v149 offset:53248
	ds_read_b128 v[206:209], v149 offset:54272
	ds_read_b128 v[210:213], v149 offset:55296
	ds_read_b128 v[214:217], v149 offset:56320
	global_load_lds_dwordx4 v[218:219], off
	s_add_i32 m0, s30, 0x2000
	s_add_u32 s26, s26, 0x40080
	v_lshl_add_u64 v[218:219], v[220:221], 0, s[12:13]
	s_addc_u32 s27, s27, 0
	s_add_i32 s30, s60, s41
	global_load_lds_dwordx4 v[218:219], off
	v_lshl_add_u64 v[218:219], s[26:27], 0, v[132:133]
	s_mov_b32 m0, s30
	s_nop 0
	global_load_lds_dwordx4 v[218:219], off
	v_lshl_add_u64 v[218:219], s[26:27], 0, v[128:129]
	s_add_i32 m0, s30, 0x2000
	s_nop 0
	global_load_lds_dwordx4 v[218:219], off
	v_lshl_add_u64 v[218:219], v[222:223], 0, s[12:13]
	s_mov_b32 m0, s47
	s_nop 0
	global_load_lds_dwordx4 v[218:219], off
	v_lshl_add_u64 v[218:219], v[224:225], 0, s[12:13]
	s_mov_b32 m0, s48
	s_nop 0
	global_load_lds_dwordx4 v[218:219], off
	s_waitcnt vmcnt(8)
	s_waitcnt lgkmcnt(0)
	s_barrier
	s_setprio 1
	s_waitcnt lgkmcnt(0)
	v_mfma_f32_16x16x32_bf16 v[60:63], v[150:153], v[182:185], v[60:63]
	v_mfma_f32_16x16x32_bf16 v[56:59], v[158:161], v[182:185], v[56:59]
	v_mfma_f32_16x16x32_bf16 v[52:55], v[150:153], v[194:197], v[52:55]
	v_mfma_f32_16x16x32_bf16 v[44:47], v[158:161], v[194:197], v[44:47]
	v_mfma_f32_16x16x32_bf16 v[36:39], v[150:153], v[202:205], v[36:39]
	v_mfma_f32_16x16x32_bf16 v[28:31], v[158:161], v[202:205], v[28:31]
	v_mfma_f32_16x16x32_bf16 v[20:23], v[150:153], v[210:213], v[20:23]
	v_mfma_f32_16x16x32_bf16 v[12:15], v[158:161], v[210:213], v[12:15]
	v_mfma_f32_16x16x32_bf16 v[60:63], v[154:157], v[190:193], v[60:63]
	v_mfma_f32_16x16x32_bf16 v[56:59], v[162:165], v[190:193], v[56:59]
	v_mfma_f32_16x16x32_bf16 v[52:55], v[154:157], v[198:201], v[52:55]
	v_mfma_f32_16x16x32_bf16 v[44:47], v[162:165], v[198:201], v[44:47]
	v_mfma_f32_16x16x32_bf16 v[36:39], v[154:157], v[206:209], v[36:39]
	v_mfma_f32_16x16x32_bf16 v[28:31], v[162:165], v[206:209], v[28:31]
	v_mfma_f32_16x16x32_bf16 v[20:23], v[154:157], v[214:217], v[20:23]
	v_mfma_f32_16x16x32_bf16 v[12:15], v[162:165], v[214:217], v[12:15]
	s_setprio 0
	s_setprio 1
	v_mfma_f32_16x16x32_bf16 v[48:51], v[166:169], v[182:185], v[48:51]
	v_mfma_f32_16x16x32_bf16 v[40:43], v[174:177], v[182:185], v[40:43]
	v_mfma_f32_16x16x32_bf16 v[32:35], v[166:169], v[194:197], v[32:35]
	v_mfma_f32_16x16x32_bf16 v[24:27], v[174:177], v[194:197], v[24:27]
	v_mfma_f32_16x16x32_bf16 v[16:19], v[166:169], v[202:205], v[16:19]
	v_mfma_f32_16x16x32_bf16 v[8:11], v[174:177], v[202:205], v[8:11]
	v_mfma_f32_16x16x32_bf16 v[4:7], v[166:169], v[210:213], v[4:7]
	v_mfma_f32_16x16x32_bf16 v[0:3], v[174:177], v[210:213], v[0:3]
	v_mfma_f32_16x16x32_bf16 v[48:51], v[170:173], v[190:193], v[48:51]
	v_mfma_f32_16x16x32_bf16 v[40:43], v[178:181], v[190:193], v[40:43]
	v_mfma_f32_16x16x32_bf16 v[32:35], v[170:173], v[198:201], v[32:35]
	v_mfma_f32_16x16x32_bf16 v[24:27], v[178:181], v[198:201], v[24:27]
	v_mfma_f32_16x16x32_bf16 v[16:19], v[170:173], v[206:209], v[16:19]
	v_mfma_f32_16x16x32_bf16 v[8:11], v[178:181], v[206:209], v[8:11]
	v_mfma_f32_16x16x32_bf16 v[4:7], v[170:173], v[214:217], v[4:7]
	v_mfma_f32_16x16x32_bf16 v[0:3], v[178:181], v[214:217], v[0:3]
	s_setprio 0
	s_barrier
	s_add_i32 s58, s58, 2
	s_add_u32 s24, s24, 0x100
	s_addc_u32 s25, s25, 0
	s_cmp_gt_u32 s58, 13
	s_cbranch_scc0 .LBB0_659
	s_add_u32 s24, s54, 0xffffff00
	s_addc_u32 s25, s55, -1
	s_andn2_b64 vcc, exec, s[10:11]
	s_cbranch_vccnz .LBB0_662
	v_mov_b32_e32 v0, 0
	s_mov_b32 s4, s14
	s_mov_b32 s3, s52
	s_mov_b64 s[6:7], s[22:23]
	s_mov_b32 s49, s53
	v_mov_b32_e32 v1, v0
	v_mov_b32_e32 v2, v0
	v_mov_b32_e32 v3, v0
	v_mov_b32_e32 v4, v0
	v_mov_b32_e32 v5, v0
	v_mov_b32_e32 v6, v0
	v_mov_b32_e32 v7, v0
	v_mov_b32_e32 v8, v0
	v_mov_b32_e32 v9, v0
	v_mov_b32_e32 v10, v0
	v_mov_b32_e32 v11, v0
	v_mov_b32_e32 v16, v0
	v_mov_b32_e32 v17, v0
	v_mov_b32_e32 v18, v0
	v_mov_b32_e32 v19, v0
	v_mov_b32_e32 v24, v0
	v_mov_b32_e32 v25, v0
	v_mov_b32_e32 v26, v0
	v_mov_b32_e32 v27, v0
	v_mov_b32_e32 v32, v0
	v_mov_b32_e32 v33, v0
	v_mov_b32_e32 v34, v0
	v_mov_b32_e32 v35, v0
	v_mov_b32_e32 v40, v0
	v_mov_b32_e32 v41, v0
	v_mov_b32_e32 v42, v0
	v_mov_b32_e32 v43, v0
	v_mov_b32_e32 v48, v0
	v_mov_b32_e32 v49, v0
	v_mov_b32_e32 v50, v0
	v_mov_b32_e32 v51, v0
	v_mov_b32_e32 v12, v0
	v_mov_b32_e32 v13, v0
	v_mov_b32_e32 v14, v0
	v_mov_b32_e32 v15, v0
	v_mov_b32_e32 v20, v0
	v_mov_b32_e32 v21, v0
	v_mov_b32_e32 v22, v0
	v_mov_b32_e32 v23, v0
	v_mov_b32_e32 v28, v0
	v_mov_b32_e32 v29, v0
	v_mov_b32_e32 v30, v0
	v_mov_b32_e32 v31, v0
	v_mov_b32_e32 v36, v0
	v_mov_b32_e32 v37, v0
	v_mov_b32_e32 v38, v0
	v_mov_b32_e32 v39, v0
	v_mov_b32_e32 v44, v0
	v_mov_b32_e32 v45, v0
	v_mov_b32_e32 v46, v0
	v_mov_b32_e32 v47, v0
	v_mov_b32_e32 v52, v0
	v_mov_b32_e32 v53, v0
	v_mov_b32_e32 v54, v0
	v_mov_b32_e32 v55, v0
	v_mov_b32_e32 v56, v0
	v_mov_b32_e32 v57, v0
	v_mov_b32_e32 v58, v0
	v_mov_b32_e32 v59, v0
	v_mov_b32_e32 v60, v0
	v_mov_b32_e32 v61, v0
	v_mov_b32_e32 v62, v0
	v_mov_b32_e32 v63, v0
	v_mov_b32_e32 v64, v0
	v_mov_b32_e32 v65, v0
	v_mov_b32_e32 v66, v0
	v_mov_b32_e32 v67, v0
	v_mov_b32_e32 v68, v0
	v_mov_b32_e32 v69, v0
	v_mov_b32_e32 v70, v0
	v_mov_b32_e32 v71, v0
	v_mov_b32_e32 v72, v0
	v_mov_b32_e32 v73, v0
	v_mov_b32_e32 v74, v0
	v_mov_b32_e32 v75, v0
	v_mov_b32_e32 v80, v0
	v_mov_b32_e32 v81, v0
	v_mov_b32_e32 v82, v0
	v_mov_b32_e32 v83, v0
	v_mov_b32_e32 v88, v0
	v_mov_b32_e32 v89, v0
	v_mov_b32_e32 v90, v0
	v_mov_b32_e32 v91, v0
	v_mov_b32_e32 v96, v0
	v_mov_b32_e32 v97, v0
	v_mov_b32_e32 v98, v0
	v_mov_b32_e32 v99, v0
	v_mov_b32_e32 v104, v0
	v_mov_b32_e32 v105, v0
	v_mov_b32_e32 v106, v0
	v_mov_b32_e32 v107, v0
	v_mov_b32_e32 v116, v0
	v_mov_b32_e32 v117, v0
	v_mov_b32_e32 v118, v0
	v_mov_b32_e32 v119, v0
	v_mov_b32_e32 v76, v0
	v_mov_b32_e32 v77, v0
	v_mov_b32_e32 v78, v0
	v_mov_b32_e32 v79, v0
	v_mov_b32_e32 v84, v0
	v_mov_b32_e32 v85, v0
	v_mov_b32_e32 v86, v0
	v_mov_b32_e32 v87, v0
	v_mov_b32_e32 v92, v0
	v_mov_b32_e32 v93, v0
	v_mov_b32_e32 v94, v0
	v_mov_b32_e32 v95, v0
	v_mov_b32_e32 v100, v0
	v_mov_b32_e32 v101, v0
	v_mov_b32_e32 v102, v0
	v_mov_b32_e32 v103, v0
	v_mov_b32_e32 v108, v0
	v_mov_b32_e32 v109, v0
	v_mov_b32_e32 v110, v0
	v_mov_b32_e32 v111, v0
	v_mov_b32_e32 v112, v0
	v_mov_b32_e32 v113, v0
	v_mov_b32_e32 v114, v0
	v_mov_b32_e32 v115, v0
	v_mov_b32_e32 v120, v0
	v_mov_b32_e32 v121, v0
	v_mov_b32_e32 v122, v0
	v_mov_b32_e32 v123, v0
	v_mov_b32_e32 v124, v0
	v_mov_b32_e32 v125, v0
	v_mov_b32_e32 v126, v0
	v_mov_b32_e32 v127, v0
	s_andn2_b64 vcc, exec, s[8:9]
	s_cbranch_vccnz .LBB0_663
	s_branch .LBB0_664
